# speedup vs baseline: 1.0060x; 1.0060x over previous
.LBB1_4:
	s_waitcnt lgkmcnt(0)
	v_pk_add_f32 v[4:5], v[40:41], v[42:43]
	v_pk_add_f32 v[2:3], v[38:39], v[2:3]
	v_or_b32_e32 v0, s2, v0
	v_pk_add_f32 v[2:3], v[4:5], v[2:3]
	v_mov_b32_e32 v1, 0
	v_add_f32_e32 v2, v2, v3
	v_lshl_add_u64 v[0:1], v[0:1], 2, s[10:11]
	global_store_dword v[0:1], v2, off
	s_endpgm
	s_nop 0
	s_nop 0
	s_nop 0
	s_nop 0
	s_nop 0
	s_nop 0
	s_nop 0
	s_nop 0
	s_nop 0
	s_nop 0
	s_nop 0
	s_nop 0
	s_nop 0
	s_nop 0
	s_nop 0
	s_nop 0
	s_nop 0
	s_nop 0
	s_nop 0
	s_nop 0
	s_nop 0
	s_nop 0
	s_nop 0
	s_nop 0
	s_nop 0
	s_nop 0
	s_nop 0
	s_nop 0
	s_nop 0
	s_nop 0
	s_nop 0
	s_endpgm

.LBB2_6:
	s_load_dwordx2 s[2:3], s[0:1], 0x0
	s_load_dwordx4 s[4:7], s[0:1], 0x10
	s_lshl_b32 s0, s10, 8
	s_lshl_b32 s1, s9, 7
	s_add_i32 s0, s1, s0
	s_ashr_i32 s1, s0, 31
	s_lshl_b64 s[0:1], s[0:1], 10
	s_waitcnt lgkmcnt(0)
	s_add_u32 s0, s2, s0
	s_addc_u32 s1, s3, s1
	v_mov_b32_e32 v131, 0
	v_lshl_add_u64 v[2:3], s[0:1], 0, v[130:131]
	global_load_dwordx4 v[4:7], v130, s[0:1]
	global_load_dwordx4 v[8:11], v130, s[0:1] offset:1024
	global_load_dwordx4 v[12:15], v130, s[0:1] offset:2048
	global_load_dwordx4 v[16:19], v130, s[0:1] offset:3072
	s_mov_b32 s0, 0x10000
	v_add_co_u32_e32 v36, vcc, s0, v2
	s_mov_b32 s0, 0x11000
	s_nop 0
	v_addc_co_u32_e32 v37, vcc, 0, v3, vcc
	v_add_co_u32_e32 v80, vcc, s0, v2
	s_lshl_b32 s0, s10, 7
	s_ashr_i32 s1, s0, 31
	v_mov_b32_e32 v1, v131
	v_lshl_add_u64 v[32:33], s[0:1], 0, v[0:1]
	v_lshlrev_b64 v[32:33], 2, v[32:33]
	v_addc_co_u32_e32 v81, vcc, 0, v3, vcc
	v_lshl_add_u64 v[34:35], s[4:5], 0, v[32:33]
	global_load_dwordx4 v[20:23], v[80:81], off offset:-4096
	global_load_dwordx4 v[24:27], v[36:37], off offset:1024
	global_load_dwordx4 v[28:31], v[36:37], off offset:2048
	global_load_dword v1, v[34:35], off offset:-1024
	v_lshl_add_u64 v[38:39], s[6:7], 0, v[32:33]
	global_load_dword v102, v[38:39], off offset:-1024
	global_load_dwordx4 v[32:35], v[36:37], off offset:3072
	s_movk_i32 s1, 0x2000
	v_add_co_u32_e32 v82, vcc, s1, v2
	s_movk_i32 s0, 0x1000
	s_nop 0
	v_addc_co_u32_e32 v83, vcc, 0, v3, vcc
	global_load_dwordx4 v[36:39], v[82:83], off offset:-4096
	v_add_co_u32_e32 v84, vcc, s0, v2
	s_mov_b32 s1, 0x13000
	s_nop 0
	v_addc_co_u32_e32 v85, vcc, 0, v3, vcc
	global_load_dwordx4 v[40:43], v[84:85], off offset:1024
	global_load_dwordx4 v[44:47], v[84:85], off offset:2048
	global_load_dwordx4 v[48:51], v[84:85], off offset:3072
	global_load_dwordx4 v[52:55], v[80:81], off
	global_load_dwordx4 v[56:59], v[80:81], off offset:1024
	global_load_dwordx4 v[60:63], v[80:81], off offset:2048
	global_load_dwordx4 v[64:67], v[80:81], off offset:3072
	global_load_dwordx4 v[68:71], v[82:83], off
	global_load_dwordx4 v[72:75], v[82:83], off offset:1024
	global_load_dwordx4 v[76:79], v[82:83], off offset:2048
	v_add_co_u32_e32 v100, vcc, s1, v2
	s_mov_b32 s0, 0x12000
	global_load_dwordx4 v[80:83], v[82:83], off offset:3072
	v_addc_co_u32_e32 v101, vcc, 0, v3, vcc
	global_load_dwordx4 v[84:87], v[100:101], off offset:-4096
	v_add_co_u32_e32 v96, vcc, s0, v2
	v_lshlrev_b32_e32 v0, 2, v0
	s_nop 0
	v_addc_co_u32_e32 v97, vcc, 0, v3, vcc
	global_load_dwordx4 v[88:91], v[96:97], off offset:1024
	global_load_dwordx4 v[92:95], v[96:97], off offset:2048
	v_lshl_or_b32 v103, s9, 13, v130
	global_load_dwordx4 v[96:99], v[96:97], off offset:3072
	s_movk_i32 s1, 0x4000
	s_movk_i32 s0, 0x3000
	s_mov_b32 s2, 0x15000
	s_waitcnt vmcnt(25)
	ds_write_b128 v103, v[4:7]
	s_waitcnt vmcnt(24)
	ds_write_b128 v103, v[8:11] offset:1024
	s_waitcnt vmcnt(23)
	ds_write_b128 v103, v[12:15] offset:2048
	s_waitcnt vmcnt(22)
	ds_write_b128 v103, v[16:19] offset:3072
	s_waitcnt vmcnt(21)
	ds_write_b128 v103, v[20:23] offset:4096
	s_waitcnt vmcnt(20)
	ds_write_b128 v103, v[24:27] offset:5120
	s_waitcnt vmcnt(19)
	ds_write_b128 v103, v[28:31] offset:6144
	s_waitcnt vmcnt(18)
	v_mul_f32_e32 v1, 0x4038aa3b, v1
	s_waitcnt vmcnt(17)
	ds_write2st64_b32 v0, v1, v102 offset0:124 offset1:126
	s_waitcnt vmcnt(16)
	ds_write_b128 v103, v[32:35] offset:7168
	v_add_co_u32_e32 v102, vcc, s1, v2
	s_waitcnt lgkmcnt(0)
	s_nop 0
	v_addc_co_u32_e32 v103, vcc, 0, v3, vcc
	v_add_co_u32_e32 v0, vcc, s0, v2
	s_barrier
	s_nop 0
	v_addc_co_u32_e32 v1, vcc, 0, v3, vcc
	global_load_dwordx4 v[4:7], v[102:103], off offset:-4096
	global_load_dwordx4 v[8:11], v[0:1], off offset:1024
	global_load_dwordx4 v[12:15], v[0:1], off offset:2048
	global_load_dwordx4 v[16:19], v[0:1], off offset:3072
	global_load_dwordx4 v[20:23], v[100:101], off
	global_load_dwordx4 v[24:27], v[100:101], off offset:1024
	global_load_dwordx4 v[28:31], v[100:101], off offset:2048
	global_load_dwordx4 v[32:35], v[100:101], off offset:3072
	s_lshl_b32 s0, s8, 13
	s_and_b32 s0, s0, 0x6000
	v_or_b32_e32 v0, s0, v130
	s_mov_b32 s1, 0x14000
	s_waitcnt vmcnt(23)
	ds_write_b128 v0, v[36:39] offset:16384
	s_waitcnt vmcnt(22)
	ds_write_b128 v0, v[40:43] offset:17408
	s_waitcnt vmcnt(21)
	ds_write_b128 v0, v[44:47] offset:18432
	s_waitcnt vmcnt(20)
	ds_write_b128 v0, v[48:51] offset:19456
	s_waitcnt vmcnt(19)
	ds_write_b128 v0, v[52:55] offset:20480
	s_waitcnt vmcnt(18)
	ds_write_b128 v0, v[56:59] offset:21504
	s_waitcnt vmcnt(17)
	ds_write_b128 v0, v[60:63] offset:22528
	s_waitcnt vmcnt(16)
	ds_write_b128 v0, v[64:67] offset:23552
	s_waitcnt lgkmcnt(0)
	s_barrier
	s_waitcnt vmcnt(15)
	ds_write_b128 v0, v[68:71]
	v_add_co_u32_e32 v68, vcc, s1, v2
	s_waitcnt vmcnt(14)
	ds_write_b128 v0, v[72:75] offset:1024
	v_addc_co_u32_e32 v69, vcc, 0, v3, vcc
	v_add_co_u32_e32 v100, vcc, s2, v2
	s_movk_i32 s0, 0x6000
	global_load_dwordx4 v[36:39], v[102:103], off
	global_load_dwordx4 v[40:43], v[102:103], off offset:1024
	global_load_dwordx4 v[44:47], v[102:103], off offset:2048
	s_waitcnt vmcnt(16)
	ds_write_b128 v0, v[76:79] offset:2048
	v_addc_co_u32_e32 v101, vcc, 0, v3, vcc
	s_waitcnt vmcnt(15)
	ds_write_b128 v0, v[80:83] offset:3072
	global_load_dwordx4 v[48:51], v[102:103], off offset:3072
	global_load_dwordx4 v[52:55], v[100:101], off offset:-4096
	s_waitcnt vmcnt(16)
	ds_write_b128 v0, v[84:87] offset:4096
	v_add_co_u32_e32 v102, vcc, s0, v2
	global_load_dwordx4 v[56:59], v[68:69], off offset:1024
	global_load_dwordx4 v[60:63], v[68:69], off offset:2048
	global_load_dwordx4 v[64:67], v[68:69], off offset:3072
	v_addc_co_u32_e32 v103, vcc, 0, v3, vcc
	s_waitcnt vmcnt(18)
	ds_write_b128 v0, v[88:91] offset:5120
	s_waitcnt vmcnt(17)
	ds_write_b128 v0, v[92:95] offset:6144
	s_waitcnt vmcnt(16)
	ds_write_b128 v0, v[96:99] offset:7168
	s_waitcnt lgkmcnt(0)
	s_barrier
	global_load_dwordx4 v[68:71], v[102:103], off offset:-4096
	s_movk_i32 s1, 0x5000
	v_add_co_u32_e32 v104, vcc, s1, v2
	s_mov_b32 s1, 0x17000
	s_nop 0
	v_addc_co_u32_e32 v105, vcc, 0, v3, vcc
	global_load_dwordx4 v[72:75], v[104:105], off offset:1024
	global_load_dwordx4 v[76:79], v[104:105], off offset:2048
	global_load_dwordx4 v[80:83], v[104:105], off offset:3072
	global_load_dwordx4 v[84:87], v[100:101], off
	global_load_dwordx4 v[88:91], v[100:101], off offset:1024
	global_load_dwordx4 v[92:95], v[100:101], off offset:2048
	global_load_dwordx4 v[96:99], v[100:101], off offset:3072
	v_add_co_u32_e32 v100, vcc, s1, v2
	s_mov_b32 s0, 0x16000
	s_nop 0
	v_addc_co_u32_e32 v101, vcc, 0, v3, vcc
	s_mov_b32 s1, 0x8000
	s_mov_b32 s2, 0xb000
	s_waitcnt vmcnt(23)
	ds_write_b128 v0, v[4:7] offset:16384
	s_waitcnt vmcnt(22)
	ds_write_b128 v0, v[8:11] offset:17408
	s_waitcnt vmcnt(21)
	ds_write_b128 v0, v[12:15] offset:18432
	s_waitcnt vmcnt(20)
	ds_write_b128 v0, v[16:19] offset:19456
	s_waitcnt vmcnt(19)
	ds_write_b128 v0, v[20:23] offset:20480
	s_waitcnt vmcnt(18)
	ds_write_b128 v0, v[24:27] offset:21504
	s_waitcnt vmcnt(17)
	ds_write_b128 v0, v[28:31] offset:22528
	s_waitcnt vmcnt(16)
	ds_write_b128 v0, v[32:35] offset:23552
	s_waitcnt lgkmcnt(0)
	s_barrier
	global_load_dwordx4 v[4:7], v[102:103], off
	global_load_dwordx4 v[8:11], v[102:103], off offset:1024
	global_load_dwordx4 v[12:15], v[102:103], off offset:2048
	global_load_dwordx4 v[16:19], v[102:103], off offset:3072
	global_load_dwordx4 v[20:23], v[100:101], off offset:-4096
	v_add_co_u32_e32 v102, vcc, s0, v2
	s_movk_i32 s0, 0x7000
	s_nop 0
	v_addc_co_u32_e32 v103, vcc, 0, v3, vcc
	global_load_dwordx4 v[24:27], v[102:103], off offset:1024
	global_load_dwordx4 v[28:31], v[102:103], off offset:2048
	global_load_dwordx4 v[32:35], v[102:103], off offset:3072
	v_add_co_u32_e32 v102, vcc, s1, v2
	s_waitcnt vmcnt(23)
	ds_write_b128 v0, v[36:39]
	s_waitcnt vmcnt(22)
	ds_write_b128 v0, v[40:43] offset:1024
	s_waitcnt vmcnt(21)
	ds_write_b128 v0, v[44:47] offset:2048
	s_waitcnt vmcnt(20)
	ds_write_b128 v0, v[48:51] offset:3072
	s_waitcnt vmcnt(19)
	ds_write_b128 v0, v[52:55] offset:4096
	s_waitcnt vmcnt(18)
	ds_write_b128 v0, v[56:59] offset:5120
	s_waitcnt vmcnt(17)
	ds_write_b128 v0, v[60:63] offset:6144
	s_waitcnt vmcnt(16)
	ds_write_b128 v0, v[64:67] offset:7168
	v_addc_co_u32_e32 v103, vcc, 0, v3, vcc
	v_add_co_u32_e32 v56, vcc, s0, v2
	s_waitcnt lgkmcnt(0)
	s_barrier
	global_load_dwordx4 v[36:39], v[102:103], off offset:-4096
	s_waitcnt vmcnt(16)
	ds_write_b128 v0, v[68:71] offset:16384
	v_addc_co_u32_e32 v57, vcc, 0, v3, vcc
	s_waitcnt vmcnt(15)
	ds_write_b128 v0, v[72:75] offset:17408
	s_waitcnt vmcnt(14)
	ds_write_b128 v0, v[76:79] offset:18432
	global_load_dwordx4 v[40:43], v[56:57], off offset:1024
	global_load_dwordx4 v[44:47], v[56:57], off offset:2048
	s_waitcnt vmcnt(15)
	ds_write_b128 v0, v[80:83] offset:19456
	global_load_dwordx4 v[48:51], v[56:57], off offset:3072
	global_load_dwordx4 v[52:55], v[100:101], off
	s_waitcnt vmcnt(16)
	ds_write_b128 v0, v[84:87] offset:20480
	s_waitcnt vmcnt(15)
	ds_write_b128 v0, v[88:91] offset:21504
	global_load_dwordx4 v[56:59], v[100:101], off offset:1024
	global_load_dwordx4 v[60:63], v[100:101], off offset:2048
	s_mov_b32 s0, 0x18000
	v_add_co_u32_e32 v84, vcc, s0, v2
	s_waitcnt vmcnt(16)
	ds_write_b128 v0, v[92:95] offset:22528
	global_load_dwordx4 v[64:67], v[100:101], off offset:3072
	s_waitcnt vmcnt(16)
	ds_write_b128 v0, v[96:99] offset:23552
	s_waitcnt lgkmcnt(0)
	s_barrier
	global_load_dwordx4 v[68:71], v[102:103], off
	global_load_dwordx4 v[72:75], v[102:103], off offset:1024
	s_mov_b32 s1, 0x19000
	v_addc_co_u32_e32 v85, vcc, 0, v3, vcc
	global_load_dwordx4 v[76:79], v[102:103], off offset:2048
	global_load_dwordx4 v[80:83], v[102:103], off offset:3072
	v_add_co_u32_e32 v100, vcc, s1, v2
	s_waitcnt vmcnt(19)
	ds_write_b128 v0, v[4:7]
	s_waitcnt vmcnt(18)
	ds_write_b128 v0, v[8:11] offset:1024
	v_addc_co_u32_e32 v101, vcc, 0, v3, vcc
	s_mov_b32 s1, 0xa000
	global_load_dwordx4 v[4:7], v[100:101], off offset:-4096
	global_load_dwordx4 v[8:11], v[84:85], off offset:1024
	s_waitcnt vmcnt(19)
	ds_write_b128 v0, v[12:15] offset:2048
	s_waitcnt vmcnt(18)
	ds_write_b128 v0, v[16:19] offset:3072
	s_waitcnt vmcnt(17)
	ds_write_b128 v0, v[20:23] offset:4096
	v_add_co_u32_e32 v102, vcc, s1, v2
	global_load_dwordx4 v[12:15], v[84:85], off offset:2048
	s_waitcnt vmcnt(17)
	ds_write_b128 v0, v[24:27] offset:5120
	s_waitcnt vmcnt(16)
	ds_write_b128 v0, v[28:31] offset:6144
	v_addc_co_u32_e32 v103, vcc, 0, v3, vcc
	global_load_dwordx4 v[16:19], v[84:85], off offset:3072
	s_waitcnt vmcnt(16)
	ds_write_b128 v0, v[32:35] offset:7168
	s_waitcnt lgkmcnt(0)
	s_barrier
	global_load_dwordx4 v[20:23], v[102:103], off offset:-4096
	s_mov_b32 s0, 0x9000
	v_add_co_u32_e32 v104, vcc, s0, v2
	s_mov_b32 s0, 0x1a000
	s_nop 0
	v_addc_co_u32_e32 v105, vcc, 0, v3, vcc
	global_load_dwordx4 v[24:27], v[104:105], off offset:1024
	global_load_dwordx4 v[28:31], v[104:105], off offset:2048
	global_load_dwordx4 v[32:35], v[104:105], off offset:3072
	global_load_dwordx4 v[84:87], v[100:101], off
	global_load_dwordx4 v[88:91], v[100:101], off offset:1024
	global_load_dwordx4 v[92:95], v[100:101], off offset:2048
	global_load_dwordx4 v[96:99], v[100:101], off offset:3072
	s_waitcnt vmcnt(23)
	ds_write_b128 v0, v[36:39] offset:16384
	s_waitcnt vmcnt(22)
	ds_write_b128 v0, v[40:43] offset:17408
	s_waitcnt vmcnt(21)
	ds_write_b128 v0, v[44:47] offset:18432
	s_waitcnt vmcnt(20)
	ds_write_b128 v0, v[48:51] offset:19456
	s_waitcnt vmcnt(19)
	ds_write_b128 v0, v[52:55] offset:20480
	s_waitcnt vmcnt(18)
	ds_write_b128 v0, v[56:59] offset:21504
	s_waitcnt vmcnt(17)
	ds_write_b128 v0, v[60:63] offset:22528
	s_waitcnt vmcnt(16)
	ds_write_b128 v0, v[64:67] offset:23552
	v_add_co_u32_e32 v56, vcc, s0, v2
	s_mov_b32 s1, 0x1b000
	s_nop 0
	v_addc_co_u32_e32 v57, vcc, 0, v3, vcc
	v_add_co_u32_e32 v64, vcc, s1, v2
	s_waitcnt lgkmcnt(0)
	s_barrier
	s_waitcnt vmcnt(15)
	ds_write_b128 v0, v[68:71]
	s_waitcnt vmcnt(14)
	ds_write_b128 v0, v[72:75] offset:1024
	v_addc_co_u32_e32 v65, vcc, 0, v3, vcc
	s_mov_b32 s0, 0xc000
	global_load_dwordx4 v[36:39], v[102:103], off offset:1024
	global_load_dwordx4 v[40:43], v[102:103], off offset:2048
	s_waitcnt vmcnt(14)
	ds_write_b128 v0, v[80:83] offset:3072
	v_add_co_u32_e32 v80, vcc, s0, v2
	ds_write_b128 v0, v[76:79] offset:2048
	s_nop 0
	v_addc_co_u32_e32 v81, vcc, 0, v3, vcc
	global_load_dwordx4 v[44:47], v[102:103], off offset:3072
	global_load_dwordx4 v[48:51], v[64:65], off offset:-4096
	v_add_co_u32_e32 v66, vcc, s2, v2
	s_mov_b32 s0, 0x1c000
	s_nop 0
	v_addc_co_u32_e32 v67, vcc, 0, v3, vcc
	v_add_co_u32_e32 v100, vcc, s0, v2
	s_mov_b32 s0, 0x1d000
	s_nop 0
	v_addc_co_u32_e32 v101, vcc, 0, v3, vcc
	s_mov_b32 s1, 0xe000
	s_waitcnt vmcnt(15)
	ds_write_b128 v0, v[4:7] offset:4096
	s_waitcnt vmcnt(14)
	ds_write_b128 v0, v[8:11] offset:5120
	global_load_dwordx4 v[4:7], v[56:57], off offset:1024
	global_load_dwordx4 v[8:11], v[56:57], off offset:2048
	s_waitcnt vmcnt(15)
	ds_write_b128 v0, v[12:15] offset:6144
	global_load_dwordx4 v[12:15], v[102:103], off
	global_load_dwordx4 v[52:55], v[56:57], off offset:3072
	v_add_co_u32_e32 v102, vcc, s0, v2
	s_waitcnt vmcnt(16)
	ds_write_b128 v0, v[16:19] offset:7168
	s_waitcnt lgkmcnt(0)
	s_barrier
	global_load_dwordx4 v[16:19], v[80:81], off offset:-4096
	global_load_dwordx4 v[56:59], v[66:67], off offset:1024
	global_load_dwordx4 v[60:63], v[66:67], off offset:2048
	s_waitcnt vmcnt(18)
	ds_write_b128 v0, v[20:23] offset:16384
	s_waitcnt vmcnt(17)
	ds_write_b128 v0, v[24:27] offset:17408
	global_load_dwordx4 v[20:23], v[66:67], off offset:3072
	s_waitcnt vmcnt(17)
	ds_write_b128 v0, v[28:31] offset:18432
	s_waitcnt vmcnt(16)
	ds_write_b128 v0, v[32:35] offset:19456
	global_load_dwordx4 v[24:27], v[64:65], off
	global_load_dwordx4 v[28:31], v[64:65], off offset:1024
	s_waitcnt vmcnt(17)
	ds_write_b128 v0, v[84:87] offset:20480
	s_waitcnt vmcnt(16)
	ds_write_b128 v0, v[88:91] offset:21504
	global_load_dwordx4 v[32:35], v[64:65], off offset:2048
	s_waitcnt vmcnt(16)
	ds_write_b128 v0, v[92:95] offset:22528
	global_load_dwordx4 v[64:67], v[64:65], off offset:3072
	s_waitcnt vmcnt(16)
	ds_write_b128 v0, v[96:99] offset:23552
	s_waitcnt lgkmcnt(0)
	s_barrier
	global_load_dwordx4 v[68:71], v[80:81], off
	global_load_dwordx4 v[72:75], v[80:81], off offset:1024
	global_load_dwordx4 v[76:79], v[80:81], off offset:2048
	v_addc_co_u32_e32 v103, vcc, 0, v3, vcc
	global_load_dwordx4 v[80:83], v[80:81], off offset:3072
	s_nop 0
	global_load_dwordx4 v[84:87], v[102:103], off offset:-4096
	global_load_dwordx4 v[88:91], v[100:101], off offset:1024
	global_load_dwordx4 v[92:95], v[100:101], off offset:2048
	global_load_dwordx4 v[96:99], v[100:101], off offset:3072
	v_add_co_u32_e32 v100, vcc, s1, v2
	s_mov_b32 s0, 0xd000
	s_nop 0
	v_addc_co_u32_e32 v101, vcc, 0, v3, vcc
	v_add_co_u32_e32 v104, vcc, s0, v2
	s_mov_b32 s0, 0x1e000
	s_nop 0
	v_addc_co_u32_e32 v105, vcc, 0, v3, vcc
	s_waitcnt vmcnt(17)
	ds_write_b128 v0, v[12:15]
	ds_write_b128 v0, v[36:39] offset:1024
	ds_write_b128 v0, v[40:43] offset:2048
	ds_write_b128 v0, v[44:47] offset:3072
	ds_write_b128 v0, v[48:51] offset:4096
	ds_write_b128 v0, v[4:7] offset:5120
	ds_write_b128 v0, v[8:11] offset:6144
	s_waitcnt vmcnt(16)
	ds_write_b128 v0, v[52:55] offset:7168
	s_waitcnt lgkmcnt(0)
	s_barrier
	s_waitcnt vmcnt(15)
	ds_write_b128 v0, v[16:19] offset:16384
	s_waitcnt vmcnt(14)
	ds_write_b128 v0, v[56:59] offset:17408
	s_waitcnt vmcnt(13)
	ds_write_b128 v0, v[60:63] offset:18432
	global_load_dwordx4 v[4:7], v[104:105], off offset:1024
	global_load_dwordx4 v[8:11], v[104:105], off offset:2048
	s_waitcnt vmcnt(14)
	ds_write_b128 v0, v[20:23] offset:19456
	global_load_dwordx4 v[12:15], v[104:105], off offset:3072
	global_load_dwordx4 v[16:19], v[102:103], off
	s_waitcnt vmcnt(15)
	ds_write_b128 v0, v[24:27] offset:20480
	s_waitcnt vmcnt(14)
	ds_write_b128 v0, v[28:31] offset:21504
	global_load_dwordx4 v[20:23], v[102:103], off offset:1024
	global_load_dwordx4 v[24:27], v[102:103], off offset:2048
	s_waitcnt vmcnt(15)
	ds_write_b128 v0, v[32:35] offset:22528
	global_load_dwordx4 v[28:31], v[100:101], off offset:-4096
	global_load_dwordx4 v[32:35], v[102:103], off offset:3072
	s_waitcnt vmcnt(16)
	ds_write_b128 v0, v[64:67] offset:23552
	s_waitcnt lgkmcnt(0)
	s_barrier
	s_waitcnt vmcnt(15)
	ds_write_b128 v0, v[68:71]
	v_add_co_u32_e32 v68, vcc, s0, v2
	s_mov_b32 s0, 0x1f000
	s_nop 0
	v_addc_co_u32_e32 v69, vcc, 0, v3, vcc
	v_add_co_u32_e32 v102, vcc, s0, v2
	global_load_dwordx4 v[36:39], v[100:101], off offset:1024
	global_load_dwordx4 v[40:43], v[100:101], off offset:2048
	s_waitcnt vmcnt(16)
	ds_write_b128 v0, v[72:75] offset:1024
	v_addc_co_u32_e32 v103, vcc, 0, v3, vcc
	s_waitcnt vmcnt(15)
	ds_write_b128 v0, v[76:79] offset:2048
	s_waitcnt vmcnt(14)
	ds_write_b128 v0, v[80:83] offset:3072
	s_mov_b32 s0, 0xf000
	global_load_dwordx4 v[44:47], v[100:101], off offset:3072
	global_load_dwordx4 v[48:51], v[102:103], off offset:-4096
	s_waitcnt vmcnt(15)
	ds_write_b128 v0, v[84:87] offset:4096
	s_waitcnt vmcnt(14)
	ds_write_b128 v0, v[88:91] offset:5120
	v_add_co_u32_e32 v2, vcc, s0, v2
	global_load_dwordx4 v[52:55], v[68:69], off offset:1024
	global_load_dwordx4 v[56:59], v[68:69], off offset:2048
	s_waitcnt vmcnt(15)
	ds_write_b128 v0, v[92:95] offset:6144
	v_addc_co_u32_e32 v3, vcc, 0, v3, vcc
	global_load_dwordx4 v[60:63], v[100:101], off
	global_load_dwordx4 v[64:67], v[68:69], off offset:3072
	s_waitcnt vmcnt(16)
	ds_write_b128 v0, v[96:99] offset:7168
	s_waitcnt lgkmcnt(0)
	s_barrier
	global_load_dwordx4 v[68:71], v[2:3], off
	global_load_dwordx4 v[72:75], v[2:3], off offset:1024
	global_load_dwordx4 v[76:79], v[2:3], off offset:2048
	global_load_dwordx4 v[80:83], v[2:3], off offset:3072
	global_load_dwordx4 v[84:87], v[102:103], off
	global_load_dwordx4 v[88:91], v[102:103], off offset:1024
	global_load_dwordx4 v[92:95], v[102:103], off offset:2048
	global_load_dwordx4 v[96:99], v[102:103], off offset:3072
	s_waitcnt vmcnt(17)
	ds_write_b128 v0, v[28:31] offset:16384
	ds_write_b128 v0, v[4:7] offset:17408
	ds_write_b128 v0, v[8:11] offset:18432
	ds_write_b128 v0, v[12:15] offset:19456
	ds_write_b128 v0, v[16:19] offset:20480
	ds_write_b128 v0, v[20:23] offset:21504
	ds_write_b128 v0, v[24:27] offset:22528
	s_waitcnt vmcnt(16)
	ds_write_b128 v0, v[32:35] offset:23552
	s_waitcnt lgkmcnt(0)
	s_barrier
	s_waitcnt vmcnt(9)
	ds_write_b128 v0, v[60:63]
	ds_write_b128 v0, v[36:39] offset:1024
	ds_write_b128 v0, v[40:43] offset:2048
	ds_write_b128 v0, v[44:47] offset:3072
	ds_write_b128 v0, v[48:51] offset:4096
	ds_write_b128 v0, v[52:55] offset:5120
	ds_write_b128 v0, v[56:59] offset:6144
	s_waitcnt vmcnt(8)
	ds_write_b128 v0, v[64:67] offset:7168
	s_waitcnt lgkmcnt(0)
	s_barrier
	s_waitcnt vmcnt(7)
	ds_write_b128 v0, v[68:71] offset:16384
	s_waitcnt vmcnt(6)
	ds_write_b128 v0, v[72:75] offset:17408
	s_waitcnt vmcnt(5)
	ds_write_b128 v0, v[76:79] offset:18432
	s_waitcnt vmcnt(4)
	ds_write_b128 v0, v[80:83] offset:19456
	s_waitcnt vmcnt(3)
	ds_write_b128 v0, v[84:87] offset:20480
	s_waitcnt vmcnt(2)
	ds_write_b128 v0, v[88:91] offset:21504
	s_waitcnt vmcnt(1)
	ds_write_b128 v0, v[92:95] offset:22528
	s_waitcnt vmcnt(0)
	ds_write_b128 v0, v[96:99] offset:23552
	s_waitcnt lgkmcnt(0)
	s_barrier
	s_endpgm
	s_nop 0
	s_nop 0
	s_nop 0
	s_nop 0
	s_nop 0
	s_nop 0
	s_nop 0
	s_nop 0
	s_nop 0
	s_nop 0
	s_nop 0
	s_nop 0
	s_nop 0
	s_nop 0
	s_nop 0
	s_nop 0
	s_nop 0
	s_nop 0
	s_nop 0
	s_nop 0
	s_nop 0
	s_nop 0
	s_nop 0
	s_nop 0
	s_nop 0
	s_nop 0
	s_nop 0
	s_nop 0
	s_endpgm
